# baseline (speedup 1.0000x reference)
.LrestB_done:
.Lgather_done:
	s_mov_b64 exec, -1
	v_add_f32_dpp v2, v2, v2 quad_perm:[1,0,3,2] row_mask:0xf bank_mask:0xf bound_ctrl:1
	s_nop 1
	v_add_f32_dpp v2, v2, v2 quad_perm:[2,3,0,1] row_mask:0xf bank_mask:0xf bound_ctrl:1
	s_nop 1
	v_add_f32_dpp v2, v2, v2 row_half_mirror row_mask:0xf bank_mask:0xf bound_ctrl:1
	s_nop 1
	v_add_f32_dpp v2, v2, v2 row_mirror row_mask:0xf bank_mask:0xf bound_ctrl:1
	s_nop 1
	v_add_f32_dpp v2, v2, v2 row_bcast:15 row_mask:0xa bank_mask:0xf
	s_nop 1
	v_add_f32_dpp v2, v2, v2 row_bcast:31 row_mask:0xc bank_mask:0xf
	s_nop 0
	v_readlane_b32 s4, v2, 63
	s_add_i32 s3, s27, s28
	v_cvt_f32_i32_e32 v3, s3
	v_lshlrev_b32_e32 v4, 3, v1
	s_mov_b64 exec, 1
	v_mov_b32_e32 v2, s4
	ds_write_b64 v4, v[2:3] offset:49152
	s_mov_b64 exec, -1
	s_waitcnt lgkmcnt(0)
	s_barrier
	s_cmp_lg_u32 s15, 0
	s_cbranch_scc1 .Lpartial_end
	v_and_b32_e32 v4, 15, v10
	v_lshlrev_b32_e32 v4, 3, v4
	ds_read_b64 v[2:3], v4 offset:49152
	s_lshl_b32 s0, s2, 3
	v_mov_b32_e32 v5, s0
	s_waitcnt lgkmcnt(0)
	v_add_f32_dpp v2, v2, v2 quad_perm:[1,0,3,2] row_mask:0xf bank_mask:0xf bound_ctrl:1
	v_add_f32_dpp v3, v3, v3 quad_perm:[1,0,3,2] row_mask:0xf bank_mask:0xf bound_ctrl:1
	s_nop 0
	v_add_f32_dpp v2, v2, v2 quad_perm:[2,3,0,1] row_mask:0xf bank_mask:0xf bound_ctrl:1
	v_add_f32_dpp v3, v3, v3 quad_perm:[2,3,0,1] row_mask:0xf bank_mask:0xf bound_ctrl:1
	s_nop 0
	v_add_f32_dpp v2, v2, v2 row_half_mirror row_mask:0xf bank_mask:0xf bound_ctrl:1
	v_add_f32_dpp v3, v3, v3 row_half_mirror row_mask:0xf bank_mask:0xf bound_ctrl:1
	s_nop 0
	v_add_f32_dpp v2, v2, v2 row_mirror row_mask:0xf bank_mask:0xf bound_ctrl:1
	v_add_f32_dpp v3, v3, v3 row_mirror row_mask:0xf bank_mask:0xf bound_ctrl:1
	s_mov_b64 exec, 1
	global_store_dwordx2 v5, v[2:3], s[24:25] sc0 sc1

.Llate_block:
	v_cmp_eq_u32_e32 vcc, 0, v0
	s_and_saveexec_b64 s[4:5], vcc
	s_cbranch_execz .Llate_end
	s_lshl_b32 s6, s2, 3
	v_mov_b32_e32 v2, 0
	v_mov_b32_e32 v3, 0
	v_mov_b32_e32 v4, s6
	s_waitcnt lgkmcnt(0)
	global_store_dwordx2 v4, v[2:3], s[24:25] sc0 sc1
